# speedup vs baseline: 1.0067x; 1.0067x over previous
.LBB1_10:
	s_andn2_b32 s38, 1, s33
	s_lshl_b32 s39, s38, 4
	s_add_i32 s39, s39, s27
	s_add_i32 s39, s39, 0x20800
	v_mov_b32_e32 v213, s39
	ds_read_b64 v[214:215], v213
	s_add_i32 s29, s28, 0x8000
	s_cmp_lg_u32 s28, 0x10000
	s_cselect_b32 s29, s29, 0
	s_add_i32 s36, s19, s29
	s_mov_b32 m0, s36
	s_nop 0
	global_load_lds_dwordx4 v199, s[16:17]
	s_add_i32 s34, s36, 0x400
	s_mov_b32 m0, s34
	s_nop 0
	global_load_lds_dwordx4 v208, s[16:17]
	s_add_u32 s34, s16, 0x2000
	s_addc_u32 s35, s17, 0
	s_add_i32 s37, s36, 0x2000
	s_mov_b32 m0, s37
	s_nop 0
	global_load_lds_dwordx4 v199, s[34:35]
	s_add_i32 s37, s36, 0x2400
	s_mov_b32 m0, s37
	s_nop 0
	global_load_lds_dwordx4 v208, s[34:35]
	s_add_u32 s34, s16, 0x4000
	s_addc_u32 s35, s17, 0
	s_add_i32 s37, s36, 0x4000
	s_mov_b32 m0, s37
	s_nop 0
	global_load_lds_dwordx4 v199, s[34:35]
	s_add_i32 s37, s36, 0x4400
	s_mov_b32 m0, s37
	s_nop 0
	global_load_lds_dwordx4 v208, s[34:35]
	s_add_u32 s16, s16, 0x6000
	s_addc_u32 s17, s17, 0
	s_add_i32 s34, s36, 0x6000
	s_mov_b32 m0, s34
	s_nop 0
	global_load_lds_dwordx4 v199, s[16:17]
	s_addk_i32 s36, 0x6400
	s_mov_b32 m0, s36
	s_nop 0
	global_load_lds_dwordx4 v208, s[16:17]
	s_andn2_b32 s16, 1, s33
	s_waitcnt lgkmcnt(0)
	v_readfirstlane_b32 s17, v214
	s_cmp_eq_u32 s33, 1
	s_cbranch_scc1 .LBB1_14
	s_cmp_eq_u32 s17, 0
	v_readfirstlane_b32 s17, v215
	s_cbranch_scc1 .LBB1_12
	v_lshl_add_u32 v213, s16, 10, v210
	ds_read_b32 v214, v213
	s_waitcnt lgkmcnt(0)
	v_pk_mul_f32 v[126:127], v[214:215], v[126:127] op_sel_hi:[0,1]
	v_pk_mul_f32 v[124:125], v[214:215], v[124:125] op_sel_hi:[0,1]
	v_pk_mul_f32 v[122:123], v[214:215], v[122:123] op_sel_hi:[0,1]
	v_pk_mul_f32 v[120:121], v[214:215], v[120:121] op_sel_hi:[0,1]
	v_pk_mul_f32 v[118:119], v[214:215], v[118:119] op_sel_hi:[0,1]
	v_pk_mul_f32 v[116:117], v[214:215], v[116:117] op_sel_hi:[0,1]
	v_pk_mul_f32 v[114:115], v[214:215], v[114:115] op_sel_hi:[0,1]
	v_pk_mul_f32 v[112:113], v[214:215], v[112:113] op_sel_hi:[0,1]
	v_pk_mul_f32 v[94:95], v[214:215], v[94:95] op_sel_hi:[0,1]
	v_pk_mul_f32 v[92:93], v[214:215], v[92:93] op_sel_hi:[0,1]
	v_pk_mul_f32 v[90:91], v[214:215], v[90:91] op_sel_hi:[0,1]
	v_pk_mul_f32 v[88:89], v[214:215], v[88:89] op_sel_hi:[0,1]
	v_pk_mul_f32 v[86:87], v[214:215], v[86:87] op_sel_hi:[0,1]
	v_pk_mul_f32 v[84:85], v[214:215], v[84:85] op_sel_hi:[0,1]
	v_pk_mul_f32 v[82:83], v[214:215], v[82:83] op_sel_hi:[0,1]
	v_pk_mul_f32 v[80:81], v[214:215], v[80:81] op_sel_hi:[0,1]
	v_pk_mul_f32 v[62:63], v[214:215], v[62:63] op_sel_hi:[0,1]
	v_pk_mul_f32 v[60:61], v[214:215], v[60:61] op_sel_hi:[0,1]
	v_pk_mul_f32 v[58:59], v[214:215], v[58:59] op_sel_hi:[0,1]
	v_pk_mul_f32 v[56:57], v[214:215], v[56:57] op_sel_hi:[0,1]
	v_pk_mul_f32 v[54:55], v[214:215], v[54:55] op_sel_hi:[0,1]
	v_pk_mul_f32 v[52:53], v[214:215], v[52:53] op_sel_hi:[0,1]
	v_pk_mul_f32 v[50:51], v[214:215], v[50:51] op_sel_hi:[0,1]
	v_pk_mul_f32 v[48:49], v[214:215], v[48:49] op_sel_hi:[0,1]
	v_pk_mul_f32 v[14:15], v[214:215], v[14:15] op_sel_hi:[0,1]
	v_pk_mul_f32 v[12:13], v[214:215], v[12:13] op_sel_hi:[0,1]
	v_pk_mul_f32 v[10:11], v[214:215], v[10:11] op_sel_hi:[0,1]
	v_pk_mul_f32 v[8:9], v[214:215], v[8:9] op_sel_hi:[0,1]
	v_pk_mul_f32 v[6:7], v[214:215], v[6:7] op_sel_hi:[0,1]
	v_pk_mul_f32 v[4:5], v[214:215], v[4:5] op_sel_hi:[0,1]
	v_pk_mul_f32 v[2:3], v[214:215], v[2:3] op_sel_hi:[0,1]
	v_pk_mul_f32 v[0:1], v[214:215], v[0:1] op_sel_hi:[0,1]
